# P9 norm: 8 more bit-trick bf16 packs -> v_cvt_pk_bf16_f32 (30 of 32 now)
# baseline (speedup 1.0000x reference)
; #define LAS __attribute__((address_space(3)))
; __device__ __forceinline__ unsigned pk2(float lo, float hi) { return f2bf(lo) | (f2bf(hi) << 16); }
; __device__ __forceinline__ void norm_mod_regs_lds2(const u32x4 (&w)[4], const LAS float* A, const LAS float* B, LAS unsigned char* lrow, int sw, unsigned char* o8row, int lane) {
;     float s = 0.f;
; #pragma unroll
;     for (int j = 0; j < 4; ++j) {
; #pragma unroll
;         for (int i = 0; i < 4; ++i) { const float a = bf_lo(w[j][i]), b = bf_hi(w[j][i]); s += a * a + b * b; } }
;     const float rstd = 1.f / sqrtf(wave_sum(s) * (1.f / DM) + EPS_);
;     const unsigned l8 = (unsigned)lane * 8u;
; #pragma unroll
;     for (int j = 0; j < 4; ++j) {
;         const f32x4 a0 = *(const LAS f32x4*)(A + 512 * j + 8 * lane), a1 = *(const LAS f32x4*)(A + 512 * j + 8 * lane + 4), b0 = *(const LAS f32x4*)(B + 512 * j + 8 * lane), b1 = *(const LAS f32x4*)(B + 512 * j + 8 * lane + 4);
;         const f32x4 h0 = {bf_lo(w[j][0]) * rstd * a0[0] + b0[0], bf_hi(w[j][0]) * rstd * a0[1] + b0[1], bf_lo(w[j][1]) * rstd * a0[2] + b0[2], bf_hi(w[j][1]) * rstd * a0[3] + b0[3]};
;         const f32x4 h1 = {bf_lo(w[j][2]) * rstd * a1[0] + b1[0], bf_hi(w[j][2]) * rstd * a1[1] + b1[1], bf_lo(w[j][3]) * rstd * a1[2] + b1[2], bf_hi(w[j][3]) * rstd * a1[3] + b1[3]};
;         u32x4 o; o.x = pk2(h0[0], h0[1]); o.y = pk2(h0[2], h0[3]); o.z = pk2(h1[0], h1[1]); o.w = pk2(h1[2], h1[3]);
;         *(LAS u32x4*)(lrow + (((lane + 64 * j) ^ sw) << 4)) = o;
;         u32x2 q8; q8.x = pg8::pack4_fp8(h0, pg8::F8_SH); q8.y = pg8::pack4_fp8(h1, pg8::F8_SH); *(u32x2*)((char*)(o8row + 512 * j) + l8) = q8;
.LBB0_1399:
	s_waitcnt vmcnt(7)
	v_and_b32_e32 v233, 0xffff0000, v115
	v_and_b32_e32 v232, 0xffff0000, v114
	v_lshlrev_b32_e32 v231, 16, v115
	v_lshlrev_b32_e32 v230, 16, v114
	v_pk_mul_f32 v[152:153], v[232:233], v[232:233]
	v_and_b32_e32 v237, 0xffff0000, v117
	v_and_b32_e32 v236, 0xffff0000, v116
	v_pk_fma_f32 v[160:161], v[230:231], v[230:231], v[152:153]
	v_lshlrev_b32_e32 v235, 16, v117
	v_lshlrev_b32_e32 v234, 16, v116
	v_pk_mul_f32 v[152:153], v[236:237], v[236:237]
	s_waitcnt vmcnt(6)
	v_and_b32_e32 v241, 0xffff0000, v119
	v_pk_fma_f32 v[214:215], v[234:235], v[234:235], v[152:153]
	v_and_b32_e32 v240, 0xffff0000, v118
	v_add_f32_e32 v160, v160, v161
	v_lshlrev_b32_e32 v239, 16, v119
	v_lshlrev_b32_e32 v238, 16, v118
	v_pk_mul_f32 v[152:153], v[240:241], v[240:241]
	v_add_f32_e32 v160, v214, v160
	v_pk_fma_f32 v[216:217], v[238:239], v[238:239], v[152:153]
	v_and_b32_e32 v245, 0xffff0000, v121
	v_and_b32_e32 v244, 0xffff0000, v120
	v_add_f32_e32 v160, v215, v160
	v_lshlrev_b32_e32 v243, 16, v121
	v_lshlrev_b32_e32 v242, 16, v120
	v_pk_mul_f32 v[152:153], v[244:245], v[244:245]
	v_add_f32_e32 v160, v216, v160
	v_pk_fma_f32 v[218:219], v[242:243], v[242:243], v[152:153]
	s_waitcnt vmcnt(5)
	v_and_b32_e32 v179, 0xffff0000, v123
	v_and_b32_e32 v178, 0xffff0000, v122
	v_add_f32_e32 v160, v217, v160
	v_lshlrev_b32_e32 v181, 16, v123
	v_lshlrev_b32_e32 v180, 16, v122
	v_pk_mul_f32 v[152:153], v[178:179], v[178:179]
	v_add_f32_e32 v160, v218, v160
	v_pk_fma_f32 v[220:221], v[180:181], v[180:181], v[152:153]
	v_and_b32_e32 v157, 0xffff0000, v125
	v_and_b32_e32 v156, 0xffff0000, v124
	v_add_f32_e32 v160, v219, v160
	v_lshlrev_b32_e32 v159, 16, v125
	v_lshlrev_b32_e32 v158, 16, v124
	v_pk_mul_f32 v[152:153], v[156:157], v[156:157]
	v_add_f32_e32 v160, v220, v160
	v_pk_fma_f32 v[222:223], v[158:159], v[158:159], v[152:153]
	s_waitcnt vmcnt(4)
	v_and_b32_e32 v153, 0xffff0000, v127
	v_and_b32_e32 v152, 0xffff0000, v126
	v_add_f32_e32 v160, v221, v160
	v_lshlrev_b32_e32 v155, 16, v127
	v_lshlrev_b32_e32 v154, 16, v126
	v_pk_mul_f32 v[224:225], v[152:153], v[152:153]
	v_add_f32_e32 v160, v222, v160
	v_and_b32_e32 v147, 0xffff0000, v129
	v_and_b32_e32 v146, 0xffff0000, v128
	v_pk_fma_f32 v[224:225], v[154:155], v[154:155], v[224:225]
	v_add_f32_e32 v160, v223, v160
	v_lshlrev_b32_e32 v149, 16, v129
	v_lshlrev_b32_e32 v148, 16, v128
	v_pk_mul_f32 v[150:151], v[146:147], v[146:147]
	v_add_f32_e32 v160, v224, v160
	v_pk_fma_f32 v[150:151], v[148:149], v[148:149], v[150:151]
	v_add_f32_e32 v160, v225, v160
	v_add_f32_e32 v150, v150, v160
	v_add_f32_e32 v150, v151, v150
	ds_bpermute_b32 v151, v183, v150
	s_add_i32 s24, s40, s27
	s_ashr_i32 s25, s24, 31
	s_lshl_b64 s[22:23], s[24:25], 11
	ds_read_b128 v[214:217], v189
	ds_read_b128 v[218:221], v189 offset:16
	s_waitcnt lgkmcnt(2)
	v_add_f32_e32 v150, v150, v151
	ds_bpermute_b32 v151, v184, v150
	ds_read_b128 v[222:225], v190
	ds_read_b128 v[226:229], v190 offset:16
	s_waitcnt lgkmcnt(4)
	v_mov_b32_e32 v246, v214
	s_waitcnt lgkmcnt(3)
	v_mov_b32_e32 v214, v218
	v_mov_b32_e32 v247, v216
	s_waitcnt lgkmcnt(2)
	v_add_f32_e32 v150, v150, v151
	ds_bpermute_b32 v151, v185, v150
	v_mov_b32_e32 v216, v215
	v_mov_b32_e32 v215, v220
	v_mov_b32_e32 v220, v219
	s_waitcnt lgkmcnt(2)
	v_mov_b32_e32 v248, v222
	s_waitcnt lgkmcnt(0)
	v_add_f32_e32 v160, v150, v151
	ds_bpermute_b32 v161, v186, v160
	v_lshl_add_u64 v[150:151], v[176:177], 0, s[22:23]
	v_mov_b32_e32 v249, v224
	v_mov_b32_e32 v224, v223
	v_mov_b32_e32 v222, v226
	s_waitcnt lgkmcnt(0)
	v_add_f32_e32 v160, v160, v161
	ds_bpermute_b32 v161, v187, v160
	v_mov_b32_e32 v223, v228
	v_mov_b32_e32 v228, v227
	s_waitcnt lgkmcnt(0)
	v_add_f32_e32 v160, v160, v161
	ds_bpermute_b32 v161, v188, v160
	s_waitcnt lgkmcnt(0)
	v_add_f32_e32 v160, v160, v161
	v_fmamk_f32 v160, v160, 0x3a000000, v195
	v_mul_f32_e32 v161, 0x4f800000, v160
	v_cmp_gt_f32_e32 vcc, s53, v160
	s_nop 1
	v_cndmask_b32_e32 v160, v160, v161, vcc
	v_sqrt_f32_e32 v161, v160
	s_nop 0
	v_add_u32_e32 v164, -1, v161
	v_fma_f32 v213, -v164, v161, v160
	v_cmp_ge_f32_e64 s[22:23], 0, v213
	v_add_u32_e32 v213, 1, v161
	s_nop 0
	v_cndmask_b32_e64 v164, v161, v164, s[22:23]
	v_fma_f32 v161, -v213, v161, v160
	v_cmp_lt_f32_e64 s[22:23], 0, v161
	s_nop 1
	v_cndmask_b32_e64 v161, v164, v213, s[22:23]
	v_mul_f32_e32 v164, 0x37800000, v161
	v_cndmask_b32_e32 v161, v161, v164, vcc
	v_cmp_class_f32_e32 vcc, v160, v196
	s_nop 1
	v_cndmask_b32_e32 v160, v161, v160, vcc
	v_div_scale_f32 v161, s[22:23], v160, v160, 1.0
	v_rcp_f32_e32 v164, v161
	s_nop 0
	v_fma_f32 v213, -v161, v164, 1.0
	v_fmac_f32_e32 v164, v213, v164
	v_div_scale_f32 v213, vcc, 1.0, v160, 1.0
	v_mul_f32_e32 v218, v213, v164
	v_fma_f32 v219, -v161, v218, v213
	v_fmac_f32_e32 v218, v219, v164
	v_fma_f32 v161, -v161, v218, v213
	v_div_fmas_f32 v161, v161, v164, v218
	v_div_fixup_f32 v160, v161, v160, 1.0
	v_pk_mul_f32 v[226:227], v[160:161], v[232:233] op_sel_hi:[0,1]
	v_pk_fma_f32 v[224:225], v[216:217], v[226:227], v[224:225]
	v_pk_mul_f32 v[216:217], v[160:161], v[234:235] op_sel_hi:[0,1]
	v_pk_mul_f32 v[218:219], v[160:161], v[230:231] op_sel_hi:[0,1]
	v_pk_fma_f32 v[214:215], v[214:215], v[216:217], v[222:223]
	v_pk_mul_f32 v[216:217], v[160:161], v[236:237] op_sel_hi:[0,1]
	v_pk_fma_f32 v[218:219], v[246:247], v[218:219], v[248:249]
	v_pk_fma_f32 v[220:221], v[220:221], v[216:217], v[228:229]
	v_cvt_pk_bf16_f32 v227, v218, v224
	v_cvt_pk_bf16_f32 v228, v219, v225
	v_cvt_pk_bf16_f32 v217, v215, v221
	v_cvt_pk_bf16_f32 v216, v214, v220
	v_med3_f32 v161, v218, s55, v210
	v_med3_f32 v164, v224, s55, v210
	v_mov_b32_e32 v218, 0
	v_cvt_pk_fp8_f32 v218, v161, v164
	v_med3_f32 v161, v219, s55, v210
	v_med3_f32 v214, v214, s55, v210
	v_med3_f32 v220, v220, s55, v210
	v_mov_b32_e32 v219, 0
	v_cvt_pk_fp8_f32 v219, v214, v220
	v_med3_f32 v164, v225, s55, v210
	v_cvt_pk_fp8_f32 v218, v161, v164 op_sel:[0,0,1]
	v_med3_f32 v161, v215, s55, v210
	v_med3_f32 v164, v221, s55, v210
	v_cvt_pk_fp8_f32 v219, v161, v164 op_sel:[0,0,1]
	v_mov_b32_e32 v215, v228
	v_mov_b32_e32 v214, v227
	ds_write_b128 v197, v[214:217]
	global_store_dwordx2 v[150:151], v[218:219], off
	ds_read_b128 v[214:217], v189 offset:2048
	ds_read_b128 v[218:221], v189 offset:2064
	ds_read_b128 v[222:225], v190 offset:2048
	ds_read_b128 v[226:229], v190 offset:2064
	v_pk_mul_f32 v[230:231], v[160:161], v[238:239] op_sel_hi:[0,1]
	s_waitcnt lgkmcnt(3)
; #define LAS __attribute__((address_space(3)))
; __device__ __forceinline__ unsigned pk2(float lo, float hi) { return f2bf(lo) | (f2bf(hi) << 16); }
; __device__ __forceinline__ void norm_mod_regs_lds2(const u32x4 (&w)[4], const LAS float* A, const LAS float* B, LAS unsigned char* lrow, int sw, unsigned char* o8row, int lane) {
;     ...
;     for (int j = 0; j < 4; ++j) {
;         const f32x4 a0 = *(const LAS f32x4*)(A + 512 * j + 8 * lane), a1 = *(const LAS f32x4*)(A + 512 * j + 8 * lane + 4), b0 = *(const LAS f32x4*)(B + 512 * j + 8 * lane), b1 = *(const LAS f32x4*)(B + 512 * j + 8 * lane + 4);
;         const f32x4 h0 = {bf_lo(w[j][0]) * rstd * a0[0] + b0[0], bf_hi(w[j][0]) * rstd * a0[1] + b0[1], bf_lo(w[j][1]) * rstd * a0[2] + b0[2], bf_hi(w[j][1]) * rstd * a0[3] + b0[3]};
;         const f32x4 h1 = {bf_lo(w[j][2]) * rstd * a1[0] + b1[0], bf_hi(w[j][2]) * rstd * a1[1] + b1[1], bf_lo(w[j][3]) * rstd * a1[2] + b1[2], bf_hi(w[j][3]) * rstd * a1[3] + b1[3]};
;         u32x4 o; o.x = pk2(h0[0], h0[1]); o.y = pk2(h0[2], h0[3]); o.z = pk2(h1[0], h1[1]); o.w = pk2(h1[2], h1[3]);
;         *(LAS u32x4*)(lrow + (((lane + 64 * j) ^ sw) << 4)) = o;
;         u32x2 q8; q8.x = pg8::pack4_fp8(h0, pg8::F8_SH); q8.y = pg8::pack4_fp8(h1, pg8::F8_SH); *(u32x2*)((char*)(o8row + 512 * j) + l8) = q8;
	s_waitcnt lgkmcnt(1)
	v_fma_f32 v230, v214, v230, v222
	v_fma_f32 v231, v216, v231, v224
	v_pk_mul_f32 v[232:233], v[160:161], v[240:241] op_sel_hi:[0,1]
	v_fma_f32 v214, v215, v232, v223
	v_fma_f32 v215, v217, v233, v225
	v_pk_mul_f32 v[216:217], v[160:161], v[242:243] op_sel_hi:[0,1]
	s_waitcnt lgkmcnt(0)
	v_fma_f32 v222, v218, v216, v226
	v_fma_f32 v223, v220, v217, v228
	v_pk_mul_f32 v[216:217], v[160:161], v[244:245] op_sel_hi:[0,1]
	v_fma_f32 v218, v219, v216, v227
	v_fma_f32 v219, v221, v217, v229
	v_cvt_pk_bf16_f32 v225, v230, v214
	v_cvt_pk_bf16_f32 v217, v223, v219
	v_cvt_pk_bf16_f32 v216, v222, v218
	v_med3_f32 v161, v230, s55, v210
	v_med3_f32 v164, v214, s55, v210
	v_mov_b32_e32 v220, 0
	v_cvt_pk_bf16_f32 v213, v231, v215
	v_cvt_pk_fp8_f32 v220, v161, v164
	v_med3_f32 v164, v215, s55, v210
	v_med3_f32 v214, v222, s55, v210
	v_med3_f32 v215, v218, s55, v210
	v_mov_b32_e32 v221, 0
	v_cvt_pk_fp8_f32 v221, v214, v215
	v_med3_f32 v161, v231, s55, v210
	v_cvt_pk_fp8_f32 v220, v161, v164 op_sel:[0,0,1]
	v_med3_f32 v161, v223, s55, v210
	v_med3_f32 v164, v219, s55, v210
	v_cvt_pk_fp8_f32 v221, v161, v164 op_sel:[0,0,1]
	v_mov_b32_e32 v215, v213
	v_mov_b32_e32 v214, v225
	ds_write_b128 v198, v[214:217]
	global_store_dwordx2 v[150:151], v[220:221], off offset:512
	ds_read_b128 v[214:217], v189 offset:4096
	ds_read_b128 v[218:221], v189 offset:4112
	ds_read_b128 v[222:225], v190 offset:4096
	ds_read_b128 v[226:229], v190 offset:4112
	v_pk_mul_f32 v[178:179], v[160:161], v[178:179] op_sel_hi:[0,1]
	s_waitcnt lgkmcnt(3)
	v_mov_b32_e32 v231, v216
	s_waitcnt lgkmcnt(1)
	v_mov_b32_e32 v233, v224
	v_fma_f32 v178, v178, v215, v223
	v_fma_f32 v179, v179, v217, v225
	v_mov_b32_e32 v215, v220
	s_waitcnt lgkmcnt(0)
	v_mov_b32_e32 v217, v228
	v_pk_mul_f32 v[156:157], v[160:161], v[156:157] op_sel_hi:[0,1]
	v_pk_mul_f32 v[180:181], v[160:161], v[180:181] op_sel_hi:[0,1]
	v_mov_b32_e32 v230, v214
	v_mov_b32_e32 v232, v222
	v_pk_mul_f32 v[158:159], v[160:161], v[158:159] op_sel_hi:[0,1]
	v_fma_f32 v156, v156, v219, v227
	v_fma_f32 v157, v157, v221, v229
	v_pk_fma_f32 v[180:181], v[180:181], v[230:231], v[232:233]
	v_fma_f32 v214, v158, v218, v226
	v_fma_f32 v215, v159, v215, v217
	v_bfe_u32 v161, v179, 16, 1
	v_cvt_pk_bf16_f32 v164, v180, v178
	v_bfe_u32 v216, v181, 16, 1
	v_cvt_pk_bf16_f32 v159, v215, v157
	v_cvt_pk_bf16_f32 v158, v214, v156
	v_med3_f32 v180, v180, s55, v210
	v_med3_f32 v213, v178, s55, v210
	v_mov_b32_e32 v178, 0
	v_add3_u32 v161, v179, v161, s54
	v_add3_u32 v216, v181, v216, s54
	v_cvt_pk_fp8_f32 v178, v180, v213
	v_med3_f32 v180, v181, s55, v210
	v_med3_f32 v181, v179, s55, v210
	v_med3_f32 v213, v214, s55, v210
	v_med3_f32 v156, v156, s55, v210
	v_mov_b32_e32 v179, 0
	v_cvt_pk_fp8_f32 v179, v213, v156
	v_med3_f32 v156, v215, s55, v210
	v_med3_f32 v157, v157, s55, v210
	v_cvt_pk_fp8_f32 v178, v180, v181 op_sel:[0,0,1]
	v_cvt_pk_fp8_f32 v179, v156, v157 op_sel:[0,0,1]
	v_lshrrev_b32_e32 v216, 16, v216
	v_and_or_b32 v157, v161, s52, v216
	v_mov_b32_e32 v156, v164
	ds_write_b128 v199, v[156:159]
	global_store_dwordx2 v[150:151], v[178:179], off offset:1024
	ds_read_b128 v[156:159], v189 offset:6144
	ds_read_b128 v[178:181], v189 offset:6160
	ds_read_b128 v[214:217], v190 offset:6144
	ds_read_b128 v[218:221], v190 offset:6160
	v_pk_mul_f32 v[152:153], v[160:161], v[152:153] op_sel_hi:[0,1]
	s_waitcnt lgkmcnt(3)
	v_mov_b32_e32 v223, v158
	s_waitcnt lgkmcnt(1)
	v_mov_b32_e32 v225, v216
	v_fma_f32 v152, v152, v157, v215
	v_fma_f32 v153, v153, v159, v217
	v_mov_b32_e32 v157, v180
	s_waitcnt lgkmcnt(0)
	v_mov_b32_e32 v159, v220
	v_pk_mul_f32 v[146:147], v[160:161], v[146:147] op_sel_hi:[0,1]
	v_pk_mul_f32 v[154:155], v[160:161], v[154:155] op_sel_hi:[0,1]
	v_mov_b32_e32 v222, v156
	v_mov_b32_e32 v224, v214
	v_pk_mul_f32 v[148:149], v[160:161], v[148:149] op_sel_hi:[0,1]
	v_fma_f32 v146, v146, v179, v219
	v_fma_f32 v147, v147, v181, v221
	v_pk_fma_f32 v[154:155], v[154:155], v[222:223], v[224:225]
	v_fma_f32 v156, v148, v178, v218
	v_fma_f32 v157, v149, v157, v159
	v_cvt_pk_bf16_f32 v159, v154, v152
	v_cvt_pk_bf16_f32 v149, v157, v147
	v_cvt_pk_bf16_f32 v148, v156, v146
	v_med3_f32 v154, v154, s55, v210
	v_med3_f32 v160, v152, s55, v210
	v_mov_b32_e32 v152, 0
	v_cvt_pk_bf16_f32 v158, v155, v153
	v_cvt_pk_fp8_f32 v152, v154, v160
	v_med3_f32 v154, v155, s55, v210
	v_med3_f32 v155, v153, s55, v210
	v_med3_f32 v156, v156, s55, v210
	v_med3_f32 v146, v146, s55, v210
	v_mov_b32_e32 v153, 0
	v_cvt_pk_fp8_f32 v153, v156, v146
	v_med3_f32 v146, v157, s55, v210
	v_med3_f32 v147, v147, s55, v210
	v_cvt_pk_fp8_f32 v152, v154, v155 op_sel:[0,0,1]
	v_cvt_pk_fp8_f32 v153, v146, v147 op_sel:[0,0,1]
	v_mov_b32_e32 v147, v158
	v_mov_b32_e32 v146, v159
	ds_write_b128 v200, v[146:149]
	global_store_dwordx2 v[150:151], v[152:153], off offset:1536
	s_waitcnt vmcnt(7)
	v_and_b32_e32 v233, 0xffff0000, v131
	v_and_b32_e32 v232, 0xffff0000, v130
	v_lshlrev_b32_e32 v231, 16, v131
	v_lshlrev_b32_e32 v230, 16, v130
	v_pk_mul_f32 v[152:153], v[232:233], v[232:233]
	v_and_b32_e32 v237, 0xffff0000, v133
	v_and_b32_e32 v236, 0xffff0000, v132
	v_pk_fma_f32 v[160:161], v[230:231], v[230:231], v[152:153]
	v_lshlrev_b32_e32 v235, 16, v133
	v_lshlrev_b32_e32 v234, 16, v132
	v_pk_mul_f32 v[152:153], v[236:237], v[236:237]
	s_waitcnt vmcnt(6)
; #define LAS __attribute__((address_space(3)))
; __device__ __forceinline__ unsigned pk2(float lo, float hi) { return f2bf(lo) | (f2bf(hi) << 16); }
; __device__ __forceinline__ void norm_mod_regs_lds2(const u32x4 (&w)[4], const LAS float* A, const LAS float* B, LAS unsigned char* lrow, int sw, unsigned char* o8row, int lane) {
;     float s = 0.f;
; #pragma unroll
;     for (int j = 0; j < 4; ++j) {
; #pragma unroll
;         for (int i = 0; i < 4; ++i) { const float a = bf_lo(w[j][i]), b = bf_hi(w[j][i]); s += a * a + b * b; } }
;     const float rstd = 1.f / sqrtf(wave_sum(s) * (1.f / DM) + EPS_);
;     const unsigned l8 = (unsigned)lane * 8u;
; #pragma unroll
;     for (int j = 0; j < 4; ++j) {
;         const f32x4 a0 = *(const LAS f32x4*)(A + 512 * j + 8 * lane), a1 = *(const LAS f32x4*)(A + 512 * j + 8 * lane + 4), b0 = *(const LAS f32x4*)(B + 512 * j + 8 * lane), b1 = *(const LAS f32x4*)(B + 512 * j + 8 * lane + 4);
;         const f32x4 h0 = {bf_lo(w[j][0]) * rstd * a0[0] + b0[0], bf_hi(w[j][0]) * rstd * a0[1] + b0[1], bf_lo(w[j][1]) * rstd * a0[2] + b0[2], bf_hi(w[j][1]) * rstd * a0[3] + b0[3]};
;         const f32x4 h1 = {bf_lo(w[j][2]) * rstd * a1[0] + b1[0], bf_hi(w[j][2]) * rstd * a1[1] + b1[1], bf_lo(w[j][3]) * rstd * a1[2] + b1[2], bf_hi(w[j][3]) * rstd * a1[3] + b1[3]};
;         u32x4 o; o.x = pk2(h0[0], h0[1]); o.y = pk2(h0[2], h0[3]); o.z = pk2(h1[0], h1[1]); o.w = pk2(h1[2], h1[3]);
;         *(LAS u32x4*)(lrow + (((lane + 64 * j) ^ sw) << 4)) = o;
;         u32x2 q8; q8.x = pg8::pack4_fp8(h0, pg8::F8_SH); q8.y = pg8::pack4_fp8(h1, pg8::F8_SH); *(u32x2*)((char*)(o8row + 512 * j) + l8) = q8;
	v_and_b32_e32 v241, 0xffff0000, v135
	v_pk_fma_f32 v[214:215], v[234:235], v[234:235], v[152:153]
	v_and_b32_e32 v240, 0xffff0000, v134
	v_add_f32_e32 v160, v160, v161
	v_lshlrev_b32_e32 v239, 16, v135
	v_lshlrev_b32_e32 v238, 16, v134
	v_pk_mul_f32 v[152:153], v[240:241], v[240:241]
	v_add_f32_e32 v160, v214, v160
	v_pk_fma_f32 v[216:217], v[238:239], v[238:239], v[152:153]
	v_and_b32_e32 v245, 0xffff0000, v137
	v_and_b32_e32 v244, 0xffff0000, v136
	v_add_f32_e32 v160, v215, v160
	v_lshlrev_b32_e32 v243, 16, v137
	v_lshlrev_b32_e32 v242, 16, v136
	v_pk_mul_f32 v[152:153], v[244:245], v[244:245]
	v_add_f32_e32 v160, v216, v160
	v_pk_fma_f32 v[218:219], v[242:243], v[242:243], v[152:153]
	s_waitcnt vmcnt(5)
	v_and_b32_e32 v179, 0xffff0000, v139
	v_and_b32_e32 v178, 0xffff0000, v138
	v_add_f32_e32 v160, v217, v160
	v_lshlrev_b32_e32 v181, 16, v139
	v_lshlrev_b32_e32 v180, 16, v138
	v_pk_mul_f32 v[152:153], v[178:179], v[178:179]
	v_add_f32_e32 v160, v218, v160
	v_pk_fma_f32 v[220:221], v[180:181], v[180:181], v[152:153]
	v_and_b32_e32 v157, 0xffff0000, v141
	v_and_b32_e32 v156, 0xffff0000, v140
	v_add_f32_e32 v160, v219, v160
	v_lshlrev_b32_e32 v159, 16, v141
	v_lshlrev_b32_e32 v158, 16, v140
	v_pk_mul_f32 v[152:153], v[156:157], v[156:157]
	v_add_f32_e32 v160, v220, v160
	v_pk_fma_f32 v[222:223], v[158:159], v[158:159], v[152:153]
	s_waitcnt vmcnt(4)
	v_and_b32_e32 v153, 0xffff0000, v143
	v_and_b32_e32 v152, 0xffff0000, v142
	v_add_f32_e32 v160, v221, v160
	v_lshlrev_b32_e32 v155, 16, v143
	v_lshlrev_b32_e32 v154, 16, v142
	v_pk_mul_f32 v[224:225], v[152:153], v[152:153]
	v_add_f32_e32 v160, v222, v160
	v_and_b32_e32 v147, 0xffff0000, v145
	v_and_b32_e32 v146, 0xffff0000, v144
	v_pk_fma_f32 v[224:225], v[154:155], v[154:155], v[224:225]
	v_add_f32_e32 v160, v223, v160
	v_lshlrev_b32_e32 v149, 16, v145
	v_lshlrev_b32_e32 v148, 16, v144
	v_pk_mul_f32 v[150:151], v[146:147], v[146:147]
	v_add_f32_e32 v160, v224, v160
	v_pk_fma_f32 v[150:151], v[148:149], v[148:149], v[150:151]
	v_add_f32_e32 v160, v225, v160
	v_add_f32_e32 v150, v150, v160
	v_add_f32_e32 v150, v151, v150
	ds_bpermute_b32 v151, v183, v150
	s_add_i32 s50, s24, 1
	s_ashr_i32 s51, s50, 31
	s_lshl_b64 s[22:23], s[50:51], 11
	ds_read_b128 v[214:217], v189
	ds_read_b128 v[218:221], v189 offset:16
	s_waitcnt lgkmcnt(2)
	v_add_f32_e32 v150, v150, v151
	ds_bpermute_b32 v151, v184, v150
	ds_read_b128 v[222:225], v190
	ds_read_b128 v[226:229], v190 offset:16
	s_waitcnt lgkmcnt(4)
	v_mov_b32_e32 v246, v214
	s_waitcnt lgkmcnt(3)
	v_mov_b32_e32 v214, v218
	v_mov_b32_e32 v247, v216
	s_waitcnt lgkmcnt(2)
	v_add_f32_e32 v150, v150, v151
	ds_bpermute_b32 v151, v185, v150
	v_mov_b32_e32 v216, v215
	v_mov_b32_e32 v215, v220
	v_mov_b32_e32 v220, v219
	s_waitcnt lgkmcnt(2)
	v_mov_b32_e32 v248, v222
	s_waitcnt lgkmcnt(0)
	v_add_f32_e32 v160, v150, v151
	ds_bpermute_b32 v161, v186, v160
	v_lshl_add_u64 v[150:151], v[176:177], 0, s[22:23]
	v_mov_b32_e32 v249, v224
	v_mov_b32_e32 v224, v223
	v_mov_b32_e32 v222, v226
	s_waitcnt lgkmcnt(0)
	v_add_f32_e32 v160, v160, v161
	ds_bpermute_b32 v161, v187, v160
	v_mov_b32_e32 v223, v228
	v_mov_b32_e32 v228, v227
	s_waitcnt lgkmcnt(0)
	v_add_f32_e32 v160, v160, v161
	ds_bpermute_b32 v161, v188, v160
	s_waitcnt lgkmcnt(0)
	v_add_f32_e32 v160, v160, v161
	v_fmamk_f32 v160, v160, 0x3a000000, v195
	v_mul_f32_e32 v161, 0x4f800000, v160
	v_cmp_gt_f32_e32 vcc, s53, v160
	s_nop 1
	v_cndmask_b32_e32 v160, v160, v161, vcc
	v_sqrt_f32_e32 v161, v160
	s_nop 0
	v_add_u32_e32 v164, -1, v161
	v_fma_f32 v213, -v164, v161, v160
	v_cmp_ge_f32_e64 s[22:23], 0, v213
	v_add_u32_e32 v213, 1, v161
	s_nop 0
	v_cndmask_b32_e64 v164, v161, v164, s[22:23]
	v_fma_f32 v161, -v213, v161, v160
	v_cmp_lt_f32_e64 s[22:23], 0, v161
	s_nop 1
	v_cndmask_b32_e64 v161, v164, v213, s[22:23]
	v_mul_f32_e32 v164, 0x37800000, v161
	v_cndmask_b32_e32 v161, v161, v164, vcc
	v_cmp_class_f32_e32 vcc, v160, v196
	s_nop 1
	v_cndmask_b32_e32 v160, v161, v160, vcc
	v_div_scale_f32 v161, s[22:23], v160, v160, 1.0
	v_rcp_f32_e32 v164, v161
	s_nop 0
	v_fma_f32 v213, -v161, v164, 1.0
	v_fmac_f32_e32 v164, v213, v164
	v_div_scale_f32 v213, vcc, 1.0, v160, 1.0
	v_mul_f32_e32 v218, v213, v164
	v_fma_f32 v219, -v161, v218, v213
	v_fmac_f32_e32 v218, v219, v164
	v_fma_f32 v161, -v161, v218, v213
	v_div_fmas_f32 v161, v161, v164, v218
	v_div_fixup_f32 v160, v161, v160, 1.0
	v_pk_mul_f32 v[226:227], v[160:161], v[232:233] op_sel_hi:[0,1]
	v_pk_fma_f32 v[224:225], v[216:217], v[226:227], v[224:225]
	v_pk_mul_f32 v[216:217], v[160:161], v[234:235] op_sel_hi:[0,1]
	v_pk_mul_f32 v[218:219], v[160:161], v[230:231] op_sel_hi:[0,1]
	v_pk_fma_f32 v[214:215], v[214:215], v[216:217], v[222:223]
	v_pk_mul_f32 v[216:217], v[160:161], v[236:237] op_sel_hi:[0,1]
	v_pk_fma_f32 v[218:219], v[246:247], v[218:219], v[248:249]
	v_pk_fma_f32 v[220:221], v[220:221], v[216:217], v[228:229]
	v_cvt_pk_bf16_f32 v227, v218, v224
	v_cvt_pk_bf16_f32 v228, v219, v225
	v_cvt_pk_bf16_f32 v217, v215, v221
	v_cvt_pk_bf16_f32 v216, v214, v220
	v_med3_f32 v161, v218, s55, v210
	v_med3_f32 v164, v224, s55, v210
	v_mov_b32_e32 v218, 0
	v_cvt_pk_fp8_f32 v218, v161, v164
	v_med3_f32 v161, v219, s55, v210
	v_med3_f32 v214, v214, s55, v210
	v_med3_f32 v220, v220, s55, v210
	v_mov_b32_e32 v219, 0
	v_cvt_pk_fp8_f32 v219, v214, v220
	v_med3_f32 v164, v225, s55, v210
	v_cvt_pk_fp8_f32 v218, v161, v164 op_sel:[0,0,1]
	v_med3_f32 v161, v215, s55, v210
	v_med3_f32 v164, v221, s55, v210
	v_cvt_pk_fp8_f32 v219, v161, v164 op_sel:[0,0,1]
	v_mov_b32_e32 v215, v228
	v_mov_b32_e32 v214, v227
	ds_write_b128 v201, v[214:217]
	global_store_dwordx2 v[150:151], v[218:219], off
	ds_read_b128 v[214:217], v189 offset:2048
	ds_read_b128 v[218:221], v189 offset:2064
	ds_read_b128 v[222:225], v190 offset:2048
	ds_read_b128 v[226:229], v190 offset:2064
	v_pk_mul_f32 v[230:231], v[160:161], v[238:239] op_sel_hi:[0,1]
	s_waitcnt lgkmcnt(3)
; #define LAS __attribute__((address_space(3)))
; __device__ __forceinline__ unsigned pk2(float lo, float hi) { return f2bf(lo) | (f2bf(hi) << 16); }
; __device__ __forceinline__ void norm_mod_regs_lds2(const u32x4 (&w)[4], const LAS float* A, const LAS float* B, LAS unsigned char* lrow, int sw, unsigned char* o8row, int lane) {
;     ...
;     for (int j = 0; j < 4; ++j) {
;         const f32x4 a0 = *(const LAS f32x4*)(A + 512 * j + 8 * lane), a1 = *(const LAS f32x4*)(A + 512 * j + 8 * lane + 4), b0 = *(const LAS f32x4*)(B + 512 * j + 8 * lane), b1 = *(const LAS f32x4*)(B + 512 * j + 8 * lane + 4);
;         const f32x4 h0 = {bf_lo(w[j][0]) * rstd * a0[0] + b0[0], bf_hi(w[j][0]) * rstd * a0[1] + b0[1], bf_lo(w[j][1]) * rstd * a0[2] + b0[2], bf_hi(w[j][1]) * rstd * a0[3] + b0[3]};
;         const f32x4 h1 = {bf_lo(w[j][2]) * rstd * a1[0] + b1[0], bf_hi(w[j][2]) * rstd * a1[1] + b1[1], bf_lo(w[j][3]) * rstd * a1[2] + b1[2], bf_hi(w[j][3]) * rstd * a1[3] + b1[3]};
;         u32x4 o; o.x = pk2(h0[0], h0[1]); o.y = pk2(h0[2], h0[3]); o.z = pk2(h1[0], h1[1]); o.w = pk2(h1[2], h1[3]);
;         *(LAS u32x4*)(lrow + (((lane + 64 * j) ^ sw) << 4)) = o;
;         u32x2 q8; q8.x = pg8::pack4_fp8(h0, pg8::F8_SH); q8.y = pg8::pack4_fp8(h1, pg8::F8_SH); *(u32x2*)((char*)(o8row + 512 * j) + l8) = q8;
; __device__ __forceinline__ void p9_fused4(Frame& F) {
;     ...
; #pragma unroll
;         for (int i = NFR; i < 32; ++i) fbr[i] = *(const bf16x8*)(wrb + (size_t)(i >> 2) * 4096 + (lo16 + (unsigned)((i & 3) * 1024)));
;         if (pass < 3) {
; #pragma unroll
;             for (int q = 0; q < 2; ++q)
; #pragma unroll
;                 for (int j = 0; j < 4; ++j) xw[q][j] = ldu16(WSP(bf16_t, WS_X1) + (size_t)(t0 + (pass + 1) * 16 + wave * 2 + q) * DM + 512 * j, lo16);
	s_waitcnt lgkmcnt(1)
	v_fma_f32 v230, v230, v214, v222
	v_fma_f32 v231, v231, v216, v224
	v_pk_mul_f32 v[232:233], v[160:161], v[240:241] op_sel_hi:[0,1]
	v_fma_f32 v214, v232, v215, v223
	v_fma_f32 v215, v233, v217, v225
	v_pk_mul_f32 v[216:217], v[160:161], v[242:243] op_sel_hi:[0,1]
	s_waitcnt lgkmcnt(0)
	v_fma_f32 v222, v216, v218, v226
	v_fma_f32 v223, v217, v220, v228
	v_pk_mul_f32 v[216:217], v[160:161], v[244:245] op_sel_hi:[0,1]
	v_fma_f32 v218, v216, v219, v227
	v_fma_f32 v219, v217, v221, v229
	v_cvt_pk_bf16_f32 v225, v230, v214
	v_cvt_pk_bf16_f32 v217, v223, v219
	v_cvt_pk_bf16_f32 v216, v222, v218
	v_med3_f32 v161, v230, s55, v210
	v_med3_f32 v164, v214, s55, v210
	v_mov_b32_e32 v220, 0
	v_cvt_pk_bf16_f32 v213, v231, v215
	v_cvt_pk_fp8_f32 v220, v161, v164
	v_med3_f32 v164, v215, s55, v210
	v_med3_f32 v214, v222, s55, v210
	v_med3_f32 v215, v218, s55, v210
	v_mov_b32_e32 v221, 0
	v_cvt_pk_fp8_f32 v221, v214, v215
	v_med3_f32 v161, v231, s55, v210
	v_cvt_pk_fp8_f32 v220, v161, v164 op_sel:[0,0,1]
	v_med3_f32 v161, v223, s55, v210
	v_med3_f32 v164, v219, s55, v210
	v_cvt_pk_fp8_f32 v221, v161, v164 op_sel:[0,0,1]
	v_mov_b32_e32 v215, v213
	v_mov_b32_e32 v214, v225
	ds_write_b128 v202, v[214:217]
	global_store_dwordx2 v[150:151], v[220:221], off offset:512
	ds_read_b128 v[214:217], v189 offset:4096
	ds_read_b128 v[218:221], v189 offset:4112
	ds_read_b128 v[222:225], v190 offset:4096
	ds_read_b128 v[226:229], v190 offset:4112
	v_pk_mul_f32 v[178:179], v[160:161], v[178:179] op_sel_hi:[0,1]
	s_waitcnt lgkmcnt(3)
	v_mov_b32_e32 v231, v216
	s_waitcnt lgkmcnt(1)
	v_mov_b32_e32 v233, v224
	v_fma_f32 v178, v178, v215, v223
	v_fma_f32 v179, v179, v217, v225
	v_mov_b32_e32 v215, v220
	s_waitcnt lgkmcnt(0)
	v_mov_b32_e32 v217, v228
	v_pk_mul_f32 v[156:157], v[160:161], v[156:157] op_sel_hi:[0,1]
	v_pk_mul_f32 v[180:181], v[160:161], v[180:181] op_sel_hi:[0,1]
	v_mov_b32_e32 v230, v214
	v_mov_b32_e32 v232, v222
	v_pk_mul_f32 v[158:159], v[160:161], v[158:159] op_sel_hi:[0,1]
	v_fma_f32 v156, v156, v219, v227
	v_fma_f32 v157, v157, v221, v229
	v_pk_fma_f32 v[180:181], v[180:181], v[230:231], v[232:233]
	v_fma_f32 v214, v158, v218, v226
	v_fma_f32 v215, v159, v215, v217
	v_bfe_u32 v161, v179, 16, 1
	v_cvt_pk_bf16_f32 v164, v180, v178
	v_bfe_u32 v216, v181, 16, 1
	v_cvt_pk_bf16_f32 v159, v215, v157
	v_cvt_pk_bf16_f32 v158, v214, v156
	v_med3_f32 v180, v180, s55, v210
	v_med3_f32 v213, v178, s55, v210
	v_mov_b32_e32 v178, 0
	v_add3_u32 v161, v179, v161, s54
	v_add3_u32 v216, v181, v216, s54
	v_cvt_pk_fp8_f32 v178, v180, v213
	v_med3_f32 v180, v181, s55, v210
	v_med3_f32 v181, v179, s55, v210
	v_med3_f32 v213, v214, s55, v210
	v_med3_f32 v156, v156, s55, v210
	v_mov_b32_e32 v179, 0
	v_cvt_pk_fp8_f32 v179, v213, v156
	v_med3_f32 v156, v215, s55, v210
	v_med3_f32 v157, v157, s55, v210
	v_cvt_pk_fp8_f32 v178, v180, v181 op_sel:[0,0,1]
	v_cvt_pk_fp8_f32 v179, v156, v157 op_sel:[0,0,1]
	v_lshrrev_b32_e32 v216, 16, v216
	v_and_or_b32 v157, v161, s52, v216
	v_mov_b32_e32 v156, v164
	ds_write_b128 v203, v[156:159]
	global_store_dwordx2 v[150:151], v[178:179], off offset:1024
	ds_read_b128 v[156:159], v189 offset:6144
	ds_read_b128 v[178:181], v189 offset:6160
	ds_read_b128 v[214:217], v190 offset:6144
	ds_read_b128 v[218:221], v190 offset:6160
	v_pk_mul_f32 v[152:153], v[160:161], v[152:153] op_sel_hi:[0,1]
	s_waitcnt lgkmcnt(3)
	v_mov_b32_e32 v223, v158
	s_waitcnt lgkmcnt(1)
	v_mov_b32_e32 v225, v216
	v_fma_f32 v152, v152, v157, v215
	v_fma_f32 v153, v153, v159, v217
	v_mov_b32_e32 v157, v180
	s_waitcnt lgkmcnt(0)
	v_mov_b32_e32 v159, v220
	v_pk_mul_f32 v[146:147], v[160:161], v[146:147] op_sel_hi:[0,1]
	v_pk_mul_f32 v[154:155], v[160:161], v[154:155] op_sel_hi:[0,1]
	v_mov_b32_e32 v222, v156
	v_mov_b32_e32 v224, v214
	v_pk_mul_f32 v[148:149], v[160:161], v[148:149] op_sel_hi:[0,1]
	v_fma_f32 v146, v146, v179, v219
	v_fma_f32 v147, v147, v181, v221
	v_pk_fma_f32 v[154:155], v[154:155], v[222:223], v[224:225]
	v_fma_f32 v156, v148, v178, v218
	v_fma_f32 v157, v149, v157, v159
	v_cvt_pk_bf16_f32 v159, v154, v152
	v_cvt_pk_bf16_f32 v149, v157, v147
	v_cvt_pk_bf16_f32 v148, v156, v146
	v_med3_f32 v154, v154, s55, v210
	v_med3_f32 v160, v152, s55, v210
	v_mov_b32_e32 v152, 0
	v_cvt_pk_bf16_f32 v158, v155, v153
	v_cvt_pk_fp8_f32 v152, v154, v160
	v_med3_f32 v154, v155, s55, v210
	v_med3_f32 v155, v153, s55, v210
	v_med3_f32 v156, v156, s55, v210
	v_med3_f32 v146, v146, s55, v210
	v_mov_b32_e32 v153, 0
	v_cvt_pk_fp8_f32 v153, v156, v146
	v_med3_f32 v146, v157, s55, v210
	v_med3_f32 v147, v147, s55, v210
	v_cvt_pk_fp8_f32 v152, v154, v155 op_sel:[0,0,1]
	v_cvt_pk_fp8_f32 v153, v146, v147 op_sel:[0,0,1]
	v_mov_b32_e32 v147, v158
	v_mov_b32_e32 v146, v159
	ds_write_b128 v204, v[146:149]
	global_store_dwordx2 v[150:151], v[152:153], off offset:1536
	global_load_dwordx4 v[146:149], v[168:169], off
	s_nop 0
	global_load_dwordx4 v[150:153], v[170:171], off
	global_load_dwordx4 v[154:157], v[172:173], off
	global_load_dwordx4 v[158:161], v[174:175], off
	s_cmp_lg_u32 s27, 48
	s_cbranch_scc0 .LBB0_1401
	s_add_i32 s22, s24, 16
	s_ashr_i32 s23, s22, 31
	s_lshl_b64 s[22:23], s[22:23], 12
	v_lshl_add_u64 v[126:127], v[166:167], 0, s[22:23]
	s_add_i32 s22, s24, 17
	s_ashr_i32 s23, s22, 31
	s_lshl_b64 s[22:23], s[22:23], 12
	v_lshl_add_u64 v[142:143], v[166:167], 0, s[22:23]
	global_load_dwordx4 v[114:117], v[126:127], off
	global_load_dwordx4 v[118:121], v[126:127], off offset:1024
	global_load_dwordx4 v[122:125], v[126:127], off offset:2048
	s_nop 0
	global_load_dwordx4 v[126:129], v[126:127], off offset:3072
	s_nop 0
	global_load_dwordx4 v[130:133], v[142:143], off
	global_load_dwordx4 v[134:137], v[142:143], off offset:1024
	global_load_dwordx4 v[138:141], v[142:143], off offset:2048
	s_nop 0
	global_load_dwordx4 v[142:145], v[142:143], off offset:3072
